# ssd_out z-gate loads issued together (counted waits) on top of previous version
# speedup vs baseline: 1.0296x; 1.0047x over previous
.LBB0_652:
	v_or_b32_e32 v73, s80, v110
	v_mov_b64_e32 v[66:67], s[68:69]
	s_mul_i32 s12, s81, 0x4800
	v_mad_u64_u32 v[66:67], s[20:21], v73, s30, v[66:67]
	v_add_u32_e32 v67, s12, v67
	v_readlane_b32 s12, v253, 50
	s_add_i32 s12, s88, s12
	s_mov_b64 s[20:21], 0x3000
	s_add_i32 s30, s12, s86
	v_lshl_add_u64 v[66:67], v[66:67], 0, s[20:21]
	s_lshl_b64 s[20:21], s[30:31], 2
	s_add_u32 s20, s6, s20
	v_lshlrev_b32_e32 v68, 1, v87
	s_addc_u32 s21, s7, s21
	v_and_b32_e32 v91, 14, v68
	global_load_dword v68, v1, s[20:21]
	ds_read_b32 v69, v109
	s_lshl_b32 s30, s12, 7
	v_ashrrev_i32_e32 v83, 31, v82
	v_lshl_add_u64 v[70:71], v[66:67], 0, s[30:31]
	v_lshrrev_b32_e32 v0, 5, v87
	s_waitcnt lgkmcnt(0)
	v_rcp_f32_e32 v69, v69
	v_lshrrev_b32_e32 v113, 3, v110
	v_readlane_b32 s12, v253, 51
	v_bitop3_b32 v0, v113, v0, 3 bitop3:0x78
	v_lshl_add_u32 v93, v0, 4, 0
	v_add_lshl_u32 v81, v82, s12, 8
	v_add3_u32 v0, v93, v81, v91
	ds_read_u16 v0, v0 offset:8192
	v_bfe_u32 v79, v87, 5, 2
	v_add_u32_e32 v107, 8, v82
	v_add_u32_e32 v106, 16, v82
	v_add_u32_e32 v104, 24, v82
	s_waitcnt lgkmcnt(0)
	v_lshlrev_b32_e32 v0, 16, v0
	v_add_u32_e32 v100, 32, v82
	v_add_u32_e32 v92, 56, v82
	v_mov_b32_e32 v72, s81
	v_cmp_gt_u32_e32 vcc, 32, v87
	s_waitcnt vmcnt(0)
	v_mul_f32_e32 v114, v68, v69
	v_lshlrev_b64 v[68:69], 1, v[82:83]
	v_lshl_add_u64 v[70:71], v[70:71], 0, v[68:69]
	v_readlane_b32 s100, v253, 52
	s_mov_b32 s101, 0
	s_add_i32 s100, s88, s100
	s_lshl_b32 s100, s100, 7
	v_lshl_add_u64 v[224:225], v[66:67], 0, s[100:101]
	v_lshl_add_u64 v[224:225], v[224:225], 0, v[68:69]
	global_load_dwordx2 v[190:191], v[70:71], off
	global_load_dwordx2 v[192:193], v[70:71], off offset:16
	global_load_dwordx2 v[194:195], v[70:71], off offset:32
	global_load_dwordx2 v[196:197], v[70:71], off offset:48
	global_load_dwordx2 v[198:199], v[70:71], off offset:64
	global_load_dwordx2 v[200:201], v[70:71], off offset:80
	global_load_dwordx2 v[202:203], v[70:71], off offset:96
	global_load_dwordx2 v[204:205], v[70:71], off offset:112
	global_load_dwordx2 v[206:207], v[224:225], off
	global_load_dwordx2 v[208:209], v[224:225], off offset:16
	global_load_dwordx2 v[212:213], v[224:225], off offset:32
	global_load_dwordx2 v[214:215], v[224:225], off offset:48
	global_load_dwordx2 v[216:217], v[224:225], off offset:64
	global_load_dwordx2 v[218:219], v[224:225], off offset:80
	global_load_dwordx2 v[220:221], v[224:225], off offset:96
	global_load_dwordx2 v[222:223], v[224:225], off offset:112
	v_fma_f32 v0, v114, v0, v50
	s_waitcnt vmcnt(15)
	v_lshlrev_b32_e32 v76, 16, v190
	v_mul_f32_e32 v50, 0xbfb8aa3b, v76
	v_exp_f32_e32 v50, v50
	v_and_b32_e32 v74, 0xffff0000, v190
	v_lshlrev_b32_e32 v77, 16, v191
	v_and_b32_e32 v75, 0xffff0000, v191
	v_add_f32_e32 v50, 1.0, v50
	v_rcp_f32_e32 v50, v50
	s_nop 0
	v_mul_f32_e32 v50, v50, v76
	v_mul_f32_e32 v78, v0, v50
	v_mul_f32_e32 v50, 0xbfb8aa3b, v74
	v_bitop3_b32 v0, v79, v113, 4 bitop3:0x36
	v_exp_f32_e32 v50, v50
	v_lshl_add_u32 v94, v0, 4, 0
	v_add3_u32 v0, v94, v81, v91
	ds_read_u16 v0, v0 offset:8448
	v_add_f32_e32 v50, 1.0, v50
	v_rcp_f32_e32 v50, v50
	s_waitcnt lgkmcnt(0)
	v_lshlrev_b32_e32 v0, 16, v0
	v_fma_f32 v0, v114, v0, v51
	v_mul_f32_e32 v50, v50, v74
	v_mul_f32_e32 v80, v0, v50
	v_mul_f32_e32 v50, 0xbfb8aa3b, v77
	v_bitop3_b32 v0, v79, v113, 8 bitop3:0x36
	v_exp_f32_e32 v50, v50
	v_lshl_add_u32 v95, v0, 4, 0
	v_add3_u32 v0, v95, v81, v91
	ds_read_u16 v0, v0 offset:8704
	v_add_f32_e32 v50, 1.0, v50
	v_rcp_f32_e32 v50, v50
	v_bfe_u32 v74, v107, 2, 2
	v_mul_f32_e32 v90, v80, v80
	s_waitcnt lgkmcnt(0)
	v_lshlrev_b32_e32 v0, 16, v0
	v_fma_f32 v0, v114, v0, v52
	v_mul_f32_e32 v50, v50, v77
	v_mul_f32_e32 v83, v0, v50
	v_mul_f32_e32 v50, 0xbfb8aa3b, v75
	v_bitop3_b32 v0, v79, v113, 12 bitop3:0x36
	v_exp_f32_e32 v50, v50
	v_lshl_add_u32 v96, v0, 4, 0
	v_add3_u32 v0, v96, v81, v91
	ds_read_u16 v0, v0 offset:8960
	v_add_f32_e32 v50, 1.0, v50
	v_rcp_f32_e32 v50, v50
	v_fmac_f32_e32 v90, v78, v78
	v_fmac_f32_e32 v90, v83, v83
	s_waitcnt lgkmcnt(0)
	v_lshlrev_b32_e32 v0, 16, v0
	v_fma_f32 v0, v114, v0, v53
	v_mul_f32_e32 v50, v50, v75
	v_mul_f32_e32 v88, v50, v0
	v_lshrrev_b32_e32 v53, 2, v107
	v_bitop3_b32 v53, v53, v113, 3 bitop3:0x6c
	v_add_lshl_u32 v75, v107, s12, 8
	v_lshl_add_u32 v108, v53, 4, 0
	v_add3_u32 v53, v108, v75, v91
	ds_read_u16 v53, v53 offset:8192
	v_fmac_f32_e32 v90, v88, v88
	s_waitcnt lgkmcnt(0)
	v_lshlrev_b32_e32 v53, 16, v53
	v_fma_f32 v53, v114, v53, v54
	s_waitcnt vmcnt(14)
	v_lshlrev_b32_e32 v0, 16, v192
	v_mul_f32_e32 v54, 0xbfb8aa3b, v0
	v_exp_f32_e32 v54, v54
	v_and_b32_e32 v50, 0xffff0000, v192
	v_lshlrev_b32_e32 v52, 16, v193
	v_and_b32_e32 v51, 0xffff0000, v193
	v_add_f32_e32 v54, 1.0, v54
	v_rcp_f32_e32 v54, v54
	s_nop 0
	v_mul_f32_e32 v0, v54, v0
	v_mul_f32_e32 v79, v53, v0
	v_mul_f32_e32 v53, 0xbfb8aa3b, v50
	v_exp_f32_e32 v53, v53
	v_bitop3_b32 v0, v74, v113, 4 bitop3:0x36
	v_lshl_add_u32 v109, v0, 4, 0
	v_add3_u32 v0, v109, v75, v91
	v_add_f32_e32 v53, 1.0, v53
	v_rcp_f32_e32 v53, v53
	ds_read_u16 v0, v0 offset:8448
	v_fmac_f32_e32 v90, v79, v79
	v_mul_f32_e32 v50, v53, v50
	v_add_lshl_u32 v53, v106, s12, 8
	v_add3_u32 v54, v93, v53, v91
	ds_read_u16 v54, v54 offset:8192
	s_waitcnt lgkmcnt(1)
	v_lshlrev_b32_e32 v0, 16, v0
	v_fma_f32 v0, v114, v0, v55
	v_mul_f32_e32 v81, v0, v50
	v_mul_f32_e32 v50, 0xbfb8aa3b, v52
	v_bitop3_b32 v0, v74, v113, 8 bitop3:0x36
	v_exp_f32_e32 v50, v50
	v_lshl_add_u32 v110, v0, 4, 0
	v_add3_u32 v0, v110, v75, v91
	ds_read_u16 v0, v0 offset:8704
	v_add_f32_e32 v50, 1.0, v50
	v_rcp_f32_e32 v50, v50
	s_waitcnt lgkmcnt(1)
	v_lshlrev_b32_e32 v54, 16, v54
	v_fma_f32 v54, v114, v54, v58
	s_waitcnt lgkmcnt(0)
	v_lshlrev_b32_e32 v0, 16, v0
	v_fma_f32 v0, v114, v0, v56
	v_mul_f32_e32 v50, v50, v52
	v_mul_f32_e32 v84, v0, v50
	v_mul_f32_e32 v50, 0xbfb8aa3b, v51
	v_bitop3_b32 v0, v74, v113, 12 bitop3:0x36
	v_exp_f32_e32 v50, v50
	v_lshl_add_u32 v111, v0, 4, 0
	v_add3_u32 v0, v111, v75, v91
	ds_read_u16 v0, v0 offset:8960
	v_add_f32_e32 v50, 1.0, v50
	v_rcp_f32_e32 v50, v50
	v_fmac_f32_e32 v90, v81, v81
	v_fmac_f32_e32 v90, v84, v84
	s_waitcnt lgkmcnt(0)
	v_lshlrev_b32_e32 v0, 16, v0
	v_fma_f32 v0, v114, v0, v57
	v_mul_f32_e32 v50, v50, v51
	v_mul_f32_e32 v89, v50, v0
	v_fmac_f32_e32 v90, v89, v89
	s_waitcnt vmcnt(13)
	v_lshlrev_b32_e32 v0, 16, v194
	v_mul_f32_e32 v55, 0xbfb8aa3b, v0
	v_exp_f32_e32 v55, v55
	v_and_b32_e32 v50, 0xffff0000, v194
	v_lshlrev_b32_e32 v52, 16, v195
	v_and_b32_e32 v51, 0xffff0000, v195
	v_add_f32_e32 v55, 1.0, v55
	v_rcp_f32_e32 v55, v55
	s_nop 0
	v_mul_f32_e32 v0, v55, v0
	v_mul_f32_e32 v74, v54, v0
	v_mul_f32_e32 v54, 0xbfb8aa3b, v50
	v_exp_f32_e32 v54, v54
	v_add3_u32 v0, v94, v53, v91
	ds_read_u16 v0, v0 offset:8448
	v_add_lshl_u32 v55, v104, s12, 8
	v_add_f32_e32 v54, 1.0, v54
	v_rcp_f32_e32 v54, v54
	v_fmac_f32_e32 v90, v74, v74
	s_waitcnt lgkmcnt(0)
	v_lshlrev_b32_e32 v0, 16, v0
	v_fma_f32 v0, v114, v0, v59
	v_mul_f32_e32 v50, v54, v50
	v_mul_f32_e32 v75, v0, v50
	v_mul_f32_e32 v50, 0xbfb8aa3b, v52
	v_exp_f32_e32 v50, v50
	v_add3_u32 v0, v95, v53, v91
	ds_read_u16 v0, v0 offset:8704
	v_bfe_u32 v54, v104, 2, 2
	v_add_f32_e32 v50, 1.0, v50
	v_rcp_f32_e32 v50, v50
	v_fmac_f32_e32 v90, v75, v75
	s_waitcnt lgkmcnt(0)
	v_lshlrev_b32_e32 v0, 16, v0
	v_fma_f32 v0, v114, v0, v60
	v_mul_f32_e32 v50, v50, v52
	v_mul_f32_e32 v76, v0, v50
	v_mul_f32_e32 v50, 0xbfb8aa3b, v51
	v_exp_f32_e32 v50, v50
	v_add3_u32 v0, v96, v53, v91
	ds_read_u16 v0, v0 offset:8960
	v_lshrrev_b32_e32 v53, 2, v104
	v_add_f32_e32 v50, 1.0, v50
	v_rcp_f32_e32 v50, v50
	v_bitop3_b32 v53, v53, v113, 3 bitop3:0x6c
	v_lshl_add_u32 v105, v53, 4, 0
	v_add3_u32 v53, v105, v55, v91
	ds_read_u16 v53, v53 offset:8192
	s_waitcnt lgkmcnt(1)
	v_lshlrev_b32_e32 v0, 16, v0
	v_fma_f32 v0, v114, v0, v61
	v_mul_f32_e32 v50, v50, v51
	v_mul_f32_e32 v77, v50, v0
	s_waitcnt lgkmcnt(0)
	v_lshlrev_b32_e32 v53, 16, v53
	v_fma_f32 v53, v114, v53, v62
	v_fmac_f32_e32 v90, v76, v76
	v_fmac_f32_e32 v90, v77, v77
	s_waitcnt vmcnt(12)
	v_lshlrev_b32_e32 v0, 16, v196
	v_mul_f32_e32 v56, 0xbfb8aa3b, v0
	v_exp_f32_e32 v56, v56
	v_and_b32_e32 v50, 0xffff0000, v196
	v_lshlrev_b32_e32 v52, 16, v197
	v_and_b32_e32 v51, 0xffff0000, v197
	v_add_f32_e32 v56, 1.0, v56
	v_rcp_f32_e32 v56, v56
	s_nop 0
	v_mul_f32_e32 v0, v56, v0
	v_mul_f32_e32 v58, v53, v0
	v_mul_f32_e32 v53, 0xbfb8aa3b, v50
	v_bitop3_b32 v0, v54, v113, 4 bitop3:0x36
	v_exp_f32_e32 v53, v53
	v_lshl_add_u32 v103, v0, 4, 0
	v_add3_u32 v0, v103, v55, v91
	ds_read_u16 v0, v0 offset:8448
	v_add_f32_e32 v53, 1.0, v53
	v_rcp_f32_e32 v53, v53
	v_fmac_f32_e32 v90, v58, v58
	s_waitcnt lgkmcnt(0)
	v_lshlrev_b32_e32 v0, 16, v0
	v_fma_f32 v0, v114, v0, v63
	v_mul_f32_e32 v50, v53, v50
	v_mul_f32_e32 v59, v0, v50
	v_mul_f32_e32 v50, 0xbfb8aa3b, v52
	v_bitop3_b32 v0, v54, v113, 8 bitop3:0x36
	v_exp_f32_e32 v50, v50
	v_lshl_add_u32 v102, v0, 4, 0
	v_add3_u32 v0, v102, v55, v91
	ds_read_u16 v0, v0 offset:8704
	v_add_f32_e32 v50, 1.0, v50
	v_rcp_f32_e32 v50, v50
	v_add_lshl_u32 v53, v100, s12, 8
	v_add_u32_e32 v63, 48, v82
	s_waitcnt lgkmcnt(0)
	v_lshlrev_b32_e32 v0, 16, v0
	v_fma_f32 v0, v114, v0, v64
	v_mul_f32_e32 v50, v50, v52
	v_mul_f32_e32 v60, v0, v50
	v_bitop3_b32 v0, v54, v113, 12 bitop3:0x36
	v_lshl_add_u32 v101, v0, 4, 0
	v_add3_u32 v0, v101, v55, v91
	ds_read_u16 v0, v0 offset:8960
	v_add3_u32 v54, v93, v53, v91
	ds_read_u16 v54, v54 offset:8192
	v_add_u32_e32 v64, 40, v82
	v_add_lshl_u32 v62, v64, s12, 8
	s_waitcnt lgkmcnt(1)
	v_lshlrev_b32_e32 v0, 16, v0
	v_fmac_f32_e32 v65, v114, v0
	v_mul_f32_e32 v0, 0xbfb8aa3b, v51
	v_exp_f32_e32 v0, v0
	s_waitcnt lgkmcnt(0)
	v_lshlrev_b32_e32 v54, 16, v54
	v_fma_f32 v34, v114, v54, v34
	v_fmac_f32_e32 v90, v59, v59
	v_add_f32_e32 v0, 1.0, v0
	v_rcp_f32_e32 v0, v0
	v_fmac_f32_e32 v90, v60, v60
	v_mul_f32_e32 v0, v0, v51
	v_mul_f32_e32 v61, v0, v65
	v_fmac_f32_e32 v90, v61, v61
	s_waitcnt vmcnt(11)
	v_lshlrev_b32_e32 v0, 16, v198
	v_mul_f32_e32 v54, 0xbfb8aa3b, v0
	v_exp_f32_e32 v54, v54
	v_and_b32_e32 v50, 0xffff0000, v198
	v_lshlrev_b32_e32 v52, 16, v199
	v_and_b32_e32 v51, 0xffff0000, v199
	v_add_f32_e32 v54, 1.0, v54
	v_rcp_f32_e32 v54, v54
	s_nop 0
	v_mul_f32_e32 v0, v54, v0
	v_mul_f32_e32 v54, v34, v0
	v_mul_f32_e32 v34, 0xbfb8aa3b, v50
	v_exp_f32_e32 v34, v34
	v_add3_u32 v0, v94, v53, v91
	ds_read_u16 v0, v0 offset:8448
	v_fmac_f32_e32 v90, v54, v54
	v_add_f32_e32 v34, 1.0, v34
	v_rcp_f32_e32 v34, v34
	s_waitcnt lgkmcnt(0)
	v_lshlrev_b32_e32 v0, 16, v0
	v_fma_f32 v0, v114, v0, v35
	v_mul_f32_e32 v34, v34, v50
	v_mul_f32_e32 v55, v0, v34
	v_mul_f32_e32 v34, 0xbfb8aa3b, v52
	v_exp_f32_e32 v34, v34
	v_add3_u32 v0, v95, v53, v91
	ds_read_u16 v0, v0 offset:8704
	v_fmac_f32_e32 v90, v55, v55
	v_add_f32_e32 v34, 1.0, v34
	v_rcp_f32_e32 v34, v34
	s_waitcnt lgkmcnt(0)
	v_lshlrev_b32_e32 v0, 16, v0
	v_fma_f32 v0, v114, v0, v36
	v_mul_f32_e32 v34, v34, v52
	v_mul_f32_e32 v56, v0, v34
	v_mul_f32_e32 v34, 0xbfb8aa3b, v51
	v_exp_f32_e32 v34, v34
	v_add3_u32 v0, v96, v53, v91
	ds_read_u16 v0, v0 offset:8960
	v_bfe_u32 v53, v64, 2, 2
	v_add_f32_e32 v34, 1.0, v34
	v_rcp_f32_e32 v34, v34
	v_fmac_f32_e32 v90, v56, v56
	s_waitcnt lgkmcnt(0)
	v_lshlrev_b32_e32 v0, 16, v0
	v_fma_f32 v0, v114, v0, v37
	v_mul_f32_e32 v34, v34, v51
	v_mul_f32_e32 v57, v34, v0
	v_lshrrev_b32_e32 v37, 2, v64
	v_bitop3_b32 v37, v37, v113, 3 bitop3:0x6c
	v_lshl_add_u32 v65, v37, 4, 0
	v_add3_u32 v37, v65, v62, v91
	ds_read_u16 v37, v37 offset:8192
	v_fmac_f32_e32 v90, v57, v57
	s_waitcnt lgkmcnt(0)
	v_lshlrev_b32_e32 v37, 16, v37
	v_fma_f32 v37, v114, v37, v38
	s_waitcnt vmcnt(10)
	v_lshlrev_b32_e32 v0, 16, v200
	v_mul_f32_e32 v38, 0xbfb8aa3b, v0
	v_exp_f32_e32 v38, v38
	v_and_b32_e32 v34, 0xffff0000, v200
	v_lshlrev_b32_e32 v36, 16, v201
	v_and_b32_e32 v35, 0xffff0000, v201
	v_add_f32_e32 v38, 1.0, v38
	v_rcp_f32_e32 v38, v38
	s_nop 0
	v_mul_f32_e32 v0, v38, v0
	v_mul_f32_e32 v50, v37, v0
	v_mul_f32_e32 v37, 0xbfb8aa3b, v34
	v_exp_f32_e32 v37, v37
	v_bitop3_b32 v0, v53, v113, 4 bitop3:0x36
	v_lshl_add_u32 v97, v0, 4, 0
	v_add3_u32 v0, v97, v62, v91
	v_add_f32_e32 v37, 1.0, v37
	v_rcp_f32_e32 v37, v37
	ds_read_u16 v0, v0 offset:8448
	v_fmac_f32_e32 v90, v50, v50
	v_mul_f32_e32 v34, v37, v34
	v_add_lshl_u32 v37, v63, s12, 8
	v_add3_u32 v38, v93, v37, v91
	ds_read_u16 v38, v38 offset:8192
	s_waitcnt lgkmcnt(1)
	v_lshlrev_b32_e32 v0, 16, v0
	v_fma_f32 v0, v114, v0, v39
	v_mul_f32_e32 v51, v0, v34
	v_mul_f32_e32 v34, 0xbfb8aa3b, v36
	v_bitop3_b32 v0, v53, v113, 8 bitop3:0x36
	v_exp_f32_e32 v34, v34
	v_lshl_add_u32 v98, v0, 4, 0
	v_add3_u32 v0, v98, v62, v91
	ds_read_u16 v0, v0 offset:8704
	v_add_f32_e32 v34, 1.0, v34
	v_rcp_f32_e32 v34, v34
	s_waitcnt lgkmcnt(1)
	v_lshlrev_b32_e32 v38, 16, v38
	v_fma_f32 v38, v114, v38, v42
	s_waitcnt lgkmcnt(0)
	v_lshlrev_b32_e32 v0, 16, v0
	v_fma_f32 v0, v114, v0, v40
	v_mul_f32_e32 v34, v34, v36
	v_mul_f32_e32 v52, v0, v34
	v_mul_f32_e32 v34, 0xbfb8aa3b, v35
	v_bitop3_b32 v0, v53, v113, 12 bitop3:0x36
	v_exp_f32_e32 v34, v34
	v_lshl_add_u32 v99, v0, 4, 0
	v_add3_u32 v0, v99, v62, v91
	ds_read_u16 v0, v0 offset:8960
	v_add_f32_e32 v34, 1.0, v34
	v_rcp_f32_e32 v34, v34
	v_fmac_f32_e32 v90, v51, v51
	v_fmac_f32_e32 v90, v52, v52
	s_waitcnt lgkmcnt(0)
	v_lshlrev_b32_e32 v0, 16, v0
	v_fma_f32 v0, v114, v0, v41
	v_mul_f32_e32 v34, v34, v35
	v_mul_f32_e32 v53, v34, v0
	v_fmac_f32_e32 v90, v53, v53
	s_waitcnt vmcnt(9)
	v_lshlrev_b32_e32 v0, 16, v202
	v_mul_f32_e32 v39, 0xbfb8aa3b, v0
	v_exp_f32_e32 v39, v39
	v_and_b32_e32 v34, 0xffff0000, v202
	v_lshlrev_b32_e32 v36, 16, v203
	v_and_b32_e32 v35, 0xffff0000, v203
	v_add_f32_e32 v39, 1.0, v39
	v_rcp_f32_e32 v39, v39
	s_nop 0
	v_mul_f32_e32 v0, v39, v0
	v_mul_f32_e32 v39, v38, v0
	v_mul_f32_e32 v38, 0xbfb8aa3b, v34
	v_exp_f32_e32 v38, v38
	v_add3_u32 v0, v94, v37, v91
	ds_read_u16 v0, v0 offset:8448
	v_fmac_f32_e32 v90, v39, v39
	v_add_f32_e32 v38, 1.0, v38
	v_rcp_f32_e32 v38, v38
	s_waitcnt lgkmcnt(0)
	v_lshlrev_b32_e32 v0, 16, v0
	v_fma_f32 v0, v114, v0, v43
	v_mul_f32_e32 v34, v38, v34
	v_mul_f32_e32 v40, v0, v34
	v_mul_f32_e32 v34, 0xbfb8aa3b, v36
	v_exp_f32_e32 v34, v34
	v_add3_u32 v0, v95, v37, v91
	ds_read_u16 v0, v0 offset:8704
	v_bfe_u32 v38, v92, 2, 2
	v_add_f32_e32 v34, 1.0, v34
	v_rcp_f32_e32 v34, v34
	v_fmac_f32_e32 v90, v40, v40
	s_waitcnt lgkmcnt(0)
	v_lshlrev_b32_e32 v0, 16, v0
	v_fma_f32 v0, v114, v0, v44
	v_mul_f32_e32 v34, v34, v36
	v_mul_f32_e32 v41, v0, v34
	v_mul_f32_e32 v34, 0xbfb8aa3b, v35
	v_exp_f32_e32 v34, v34
	v_add3_u32 v0, v96, v37, v91
	ds_read_u16 v0, v0 offset:8960
	v_lshrrev_b32_e32 v36, 2, v92
	v_add_f32_e32 v34, 1.0, v34
	v_rcp_f32_e32 v34, v34
	v_bitop3_b32 v36, v36, v113, 3 bitop3:0x6c
	s_waitcnt lgkmcnt(0)
	v_lshlrev_b32_e32 v0, 16, v0
	v_fma_f32 v0, v114, v0, v45
	v_mul_f32_e32 v34, v34, v35
	v_mul_f32_e32 v42, v34, v0
	v_add_lshl_u32 v70, v92, s12, 8
	v_lshl_add_u32 v62, v36, 4, 0
	v_add3_u32 v36, v62, v70, v91
	ds_read_u16 v36, v36 offset:8192
	v_readlane_b32 s12, v253, 52
	s_add_i32 s20, s88, s12
	s_add_i32 s30, s20, s86
	s_lshl_b64 s[38:39], s[30:31], 2
	s_waitcnt lgkmcnt(0)
	v_lshlrev_b32_e32 v36, 16, v36
	v_fma_f32 v36, v114, v36, v46
	s_add_u32 s38, s6, s38
	s_addc_u32 s39, s7, s39
	s_lshl_b32 s30, s20, 7
	v_readlane_b32 s12, v253, 53
	v_fmac_f32_e32 v90, v41, v41
	v_fmac_f32_e32 v90, v42, v42
	s_waitcnt vmcnt(8)
	v_lshlrev_b32_e32 v0, 16, v204
	v_mul_f32_e32 v43, 0xbfb8aa3b, v0
	v_exp_f32_e32 v43, v43
	v_and_b32_e32 v34, 0xffff0000, v204
	v_lshlrev_b32_e32 v37, 16, v205
	v_and_b32_e32 v35, 0xffff0000, v205
	v_add_f32_e32 v43, 1.0, v43
	v_rcp_f32_e32 v43, v43
	s_nop 0
	v_mul_f32_e32 v0, v43, v0
	v_mul_f32_e32 v43, 0xbfb8aa3b, v34
	v_mul_f32_e32 v0, v36, v0
	v_bitop3_b32 v36, v38, v113, 4 bitop3:0x36
	v_exp_f32_e32 v43, v43
	v_lshl_add_u32 v45, v36, 4, 0
	v_add3_u32 v36, v45, v70, v91
	ds_read_u16 v36, v36 offset:8448
	v_add_f32_e32 v43, 1.0, v43
	v_rcp_f32_e32 v43, v43
	v_fmac_f32_e32 v90, v0, v0
	s_waitcnt lgkmcnt(0)
	v_lshlrev_b32_e32 v36, 16, v36
	v_fma_f32 v36, v114, v36, v47
	v_mul_f32_e32 v34, v43, v34
	v_mul_f32_e32 v43, 0xbfb8aa3b, v37
	v_mul_f32_e32 v36, v36, v34
	v_bitop3_b32 v34, v38, v113, 8 bitop3:0x36
	v_exp_f32_e32 v43, v43
	v_lshl_add_u32 v44, v34, 4, 0
	v_add3_u32 v34, v44, v70, v91
	ds_read_u16 v34, v34 offset:8704
	v_add_f32_e32 v43, 1.0, v43
	v_rcp_f32_e32 v43, v43
	v_fmac_f32_e32 v90, v36, v36
	s_waitcnt lgkmcnt(0)
	v_lshlrev_b32_e32 v34, 16, v34
	v_fma_f32 v34, v114, v34, v48
	v_mul_f32_e32 v37, v43, v37
	v_mul_f32_e32 v37, v34, v37
	v_bitop3_b32 v34, v38, v113, 12 bitop3:0x36
	v_lshl_add_u32 v43, v34, 4, 0
	v_add3_u32 v34, v43, v70, v91
	ds_read_u16 v34, v34 offset:8960
	v_fmac_f32_e32 v90, v37, v37
	s_waitcnt lgkmcnt(0)
	v_lshlrev_b32_e32 v34, 16, v34
	v_fmac_f32_e32 v49, v114, v34
	v_mul_f32_e32 v34, 0xbfb8aa3b, v35
	v_exp_f32_e32 v34, v34
	s_nop 0
	v_add_f32_e32 v34, 1.0, v34
	v_rcp_f32_e32 v34, v34
	s_nop 0
	v_mul_f32_e32 v34, v34, v35
	v_mul_f32_e32 v38, v34, v49
	global_load_dword v34, v1, s[38:39]
	ds_read_b32 v35, v112
	v_fmac_f32_e32 v90, v38, v38
	s_waitcnt lgkmcnt(0)
	v_rcp_f32_e32 v35, v35
	s_waitcnt vmcnt(0)
	v_mul_f32_e32 v46, v34, v35
	v_lshl_add_u64 v[34:35], v[66:67], 0, s[30:31]
	v_lshl_add_u64 v[34:35], v[34:35], 0, v[68:69]
	v_add_lshl_u32 v67, v82, s12, 8
	v_add3_u32 v68, v93, v67, v91
	ds_read_u16 v68, v68 offset:8192
	s_waitcnt lgkmcnt(0)
	v_lshlrev_b32_e32 v68, 16, v68
	v_fma_f32 v18, v46, v68, v18
	s_waitcnt vmcnt(8)
	v_lshlrev_b32_e32 v47, 16, v206
	v_mul_f32_e32 v68, 0xbfb8aa3b, v47
	v_exp_f32_e32 v68, v68
	v_and_b32_e32 v48, 0xffff0000, v206
	v_lshlrev_b32_e32 v66, 16, v207
	v_and_b32_e32 v49, 0xffff0000, v207
	v_add_f32_e32 v68, 1.0, v68
	v_rcp_f32_e32 v68, v68
	s_nop 0
	v_mul_f32_e32 v47, v68, v47
	v_mul_f32_e32 v18, v18, v47
	v_add3_u32 v47, v94, v67, v91
	ds_read_u16 v47, v47 offset:8448
	v_fmac_f32_e32 v90, v18, v18
	s_waitcnt lgkmcnt(0)
	v_lshlrev_b32_e32 v47, 16, v47
	v_fma_f32 v19, v46, v47, v19
	v_mul_f32_e32 v47, 0xbfb8aa3b, v48
	v_exp_f32_e32 v47, v47
	s_nop 0
	v_add_f32_e32 v47, 1.0, v47
	v_rcp_f32_e32 v47, v47
	s_nop 0
	v_mul_f32_e32 v47, v47, v48
	v_mul_f32_e32 v19, v19, v47
	v_add3_u32 v47, v95, v67, v91
	ds_read_u16 v47, v47 offset:8704
	v_fmac_f32_e32 v90, v19, v19
	s_waitcnt lgkmcnt(0)
	v_lshlrev_b32_e32 v47, 16, v47
	v_fma_f32 v20, v46, v47, v20
	v_mul_f32_e32 v47, 0xbfb8aa3b, v66
	v_exp_f32_e32 v47, v47
	s_nop 0
	v_add_f32_e32 v47, 1.0, v47
	v_rcp_f32_e32 v47, v47
	s_nop 0
	v_mul_f32_e32 v47, v47, v66
	v_mul_f32_e32 v20, v20, v47
	v_add3_u32 v47, v96, v67, v91
	ds_read_u16 v47, v47 offset:8960
	v_add_lshl_u32 v67, v107, s12, 8
	v_add3_u32 v68, v108, v67, v91
	ds_read_u16 v68, v68 offset:8192
	v_fmac_f32_e32 v90, v20, v20
	s_waitcnt lgkmcnt(1)
	v_lshlrev_b32_e32 v47, 16, v47
	v_fma_f32 v21, v46, v47, v21
	v_mul_f32_e32 v47, 0xbfb8aa3b, v49
	v_exp_f32_e32 v47, v47
	s_waitcnt lgkmcnt(0)
	v_lshlrev_b32_e32 v68, 16, v68
	v_fma_f32 v22, v46, v68, v22
	v_add_f32_e32 v47, 1.0, v47
	v_rcp_f32_e32 v47, v47
	s_nop 0
	v_mul_f32_e32 v47, v47, v49
	v_mul_f32_e32 v21, v47, v21
	v_fmac_f32_e32 v90, v21, v21
	s_waitcnt vmcnt(7)
	v_lshlrev_b32_e32 v47, 16, v208
	v_mul_f32_e32 v68, 0xbfb8aa3b, v47
	v_exp_f32_e32 v68, v68
	v_and_b32_e32 v48, 0xffff0000, v208
	v_lshlrev_b32_e32 v66, 16, v209
	v_and_b32_e32 v49, 0xffff0000, v209
	v_add_f32_e32 v68, 1.0, v68
	v_rcp_f32_e32 v68, v68
	s_nop 0
	v_mul_f32_e32 v47, v68, v47
	v_mul_f32_e32 v22, v22, v47
	v_add3_u32 v47, v109, v67, v91
	ds_read_u16 v47, v47 offset:8448
	v_fmac_f32_e32 v90, v22, v22
	s_waitcnt lgkmcnt(0)
	v_lshlrev_b32_e32 v47, 16, v47
	v_fma_f32 v23, v46, v47, v23
	v_mul_f32_e32 v47, 0xbfb8aa3b, v48
	v_exp_f32_e32 v47, v47
	s_nop 0
	v_add_f32_e32 v47, 1.0, v47
	v_rcp_f32_e32 v47, v47
	s_nop 0
	v_mul_f32_e32 v47, v47, v48
	v_mul_f32_e32 v23, v23, v47
	v_add3_u32 v47, v110, v67, v91
	ds_read_u16 v47, v47 offset:8704
	v_fmac_f32_e32 v90, v23, v23
	s_waitcnt lgkmcnt(0)
	v_lshlrev_b32_e32 v47, 16, v47
	v_fma_f32 v24, v46, v47, v24
	v_mul_f32_e32 v47, 0xbfb8aa3b, v66
	v_exp_f32_e32 v47, v47
	s_nop 0
	v_add_f32_e32 v47, 1.0, v47
	v_rcp_f32_e32 v47, v47
	s_nop 0
	v_mul_f32_e32 v47, v47, v66
	v_mul_f32_e32 v24, v24, v47
	v_add3_u32 v47, v111, v67, v91
	ds_read_u16 v47, v47 offset:8960
	v_add_lshl_u32 v67, v106, s12, 8
	v_add3_u32 v68, v93, v67, v91
	ds_read_u16 v68, v68 offset:8192
	v_fmac_f32_e32 v90, v24, v24
	s_waitcnt lgkmcnt(1)
	v_lshlrev_b32_e32 v47, 16, v47
	v_fma_f32 v25, v46, v47, v25
	v_mul_f32_e32 v47, 0xbfb8aa3b, v49
	v_exp_f32_e32 v47, v47
	s_waitcnt lgkmcnt(0)
	v_lshlrev_b32_e32 v68, 16, v68
	v_fma_f32 v26, v46, v68, v26
	v_add_f32_e32 v47, 1.0, v47
	v_rcp_f32_e32 v47, v47
	s_nop 0
	v_mul_f32_e32 v47, v47, v49
	v_mul_f32_e32 v25, v47, v25
	v_fmac_f32_e32 v90, v25, v25
	s_waitcnt vmcnt(6)
	v_lshlrev_b32_e32 v47, 16, v212
	v_mul_f32_e32 v68, 0xbfb8aa3b, v47
	v_exp_f32_e32 v68, v68
	v_and_b32_e32 v48, 0xffff0000, v212
	v_lshlrev_b32_e32 v66, 16, v213
	v_and_b32_e32 v49, 0xffff0000, v213
	v_add_f32_e32 v68, 1.0, v68
	v_rcp_f32_e32 v68, v68
	s_nop 0
	v_mul_f32_e32 v47, v68, v47
	v_mul_f32_e32 v26, v26, v47
	v_add3_u32 v47, v94, v67, v91
	ds_read_u16 v47, v47 offset:8448
	v_fmac_f32_e32 v90, v26, v26
	s_waitcnt lgkmcnt(0)
	v_lshlrev_b32_e32 v47, 16, v47
	v_fma_f32 v27, v46, v47, v27
	v_mul_f32_e32 v47, 0xbfb8aa3b, v48
	v_exp_f32_e32 v47, v47
	s_nop 0
	v_add_f32_e32 v47, 1.0, v47
	v_rcp_f32_e32 v47, v47
	s_nop 0
	v_mul_f32_e32 v47, v47, v48
	v_mul_f32_e32 v27, v27, v47
	v_add3_u32 v47, v95, v67, v91
	ds_read_u16 v47, v47 offset:8704
	v_fmac_f32_e32 v90, v27, v27
	s_waitcnt lgkmcnt(0)
	v_lshlrev_b32_e32 v47, 16, v47
	v_fma_f32 v28, v46, v47, v28
	v_mul_f32_e32 v47, 0xbfb8aa3b, v66
	v_exp_f32_e32 v47, v47
	s_nop 0
	v_add_f32_e32 v47, 1.0, v47
	v_rcp_f32_e32 v47, v47
	s_nop 0
	v_mul_f32_e32 v47, v47, v66
	v_mul_f32_e32 v28, v28, v47
	v_add3_u32 v47, v96, v67, v91
	ds_read_u16 v47, v47 offset:8960
	v_add_lshl_u32 v67, v104, s12, 8
	v_add3_u32 v68, v105, v67, v91
	ds_read_u16 v68, v68 offset:8192
	v_fmac_f32_e32 v90, v28, v28
	s_waitcnt lgkmcnt(1)
	v_lshlrev_b32_e32 v47, 16, v47
	v_fma_f32 v29, v46, v47, v29
	v_mul_f32_e32 v47, 0xbfb8aa3b, v49
	v_exp_f32_e32 v47, v47
	s_waitcnt lgkmcnt(0)
	v_lshlrev_b32_e32 v68, 16, v68
	v_fma_f32 v30, v46, v68, v30
	v_add_f32_e32 v47, 1.0, v47
	v_rcp_f32_e32 v47, v47
	s_nop 0
	v_mul_f32_e32 v47, v47, v49
	v_mul_f32_e32 v29, v47, v29
	v_fmac_f32_e32 v90, v29, v29
	s_waitcnt vmcnt(5)
	v_lshlrev_b32_e32 v47, 16, v214
	v_mul_f32_e32 v68, 0xbfb8aa3b, v47
	v_exp_f32_e32 v68, v68
	v_and_b32_e32 v48, 0xffff0000, v214
	v_lshlrev_b32_e32 v66, 16, v215
	v_and_b32_e32 v49, 0xffff0000, v215
	v_add_f32_e32 v68, 1.0, v68
	v_rcp_f32_e32 v68, v68
	s_nop 0
	v_mul_f32_e32 v47, v68, v47
	v_mul_f32_e32 v30, v30, v47
	v_add3_u32 v47, v103, v67, v91
	ds_read_u16 v47, v47 offset:8448
	v_add_lshl_u32 v68, v100, s12, 8
	v_fmac_f32_e32 v90, v30, v30
	s_waitcnt lgkmcnt(0)
	v_lshlrev_b32_e32 v47, 16, v47
	v_fma_f32 v31, v46, v47, v31
	v_mul_f32_e32 v47, 0xbfb8aa3b, v48
	v_exp_f32_e32 v47, v47
	s_nop 0
	v_add_f32_e32 v47, 1.0, v47
	v_rcp_f32_e32 v47, v47
	s_nop 0
	v_mul_f32_e32 v47, v47, v48
	v_mul_f32_e32 v31, v31, v47
	v_add3_u32 v47, v102, v67, v91
	ds_read_u16 v47, v47 offset:8704
	v_fmac_f32_e32 v90, v31, v31
	s_waitcnt lgkmcnt(0)
	v_lshlrev_b32_e32 v47, 16, v47
	v_fma_f32 v32, v46, v47, v32
	v_mul_f32_e32 v47, 0xbfb8aa3b, v66
	v_exp_f32_e32 v47, v47
	s_nop 0
	v_add_f32_e32 v47, 1.0, v47
	v_rcp_f32_e32 v47, v47
	s_nop 0
	v_mul_f32_e32 v47, v47, v66
	v_mul_f32_e32 v32, v32, v47
	v_add3_u32 v47, v101, v67, v91
	ds_read_u16 v47, v47 offset:8960
	v_fmac_f32_e32 v90, v32, v32
	s_waitcnt lgkmcnt(0)
	v_lshlrev_b32_e32 v47, 16, v47
	v_fmac_f32_e32 v33, v46, v47
	v_mul_f32_e32 v47, 0xbfb8aa3b, v49
	v_exp_f32_e32 v47, v47
	s_nop 0
	v_add_f32_e32 v47, 1.0, v47
	v_rcp_f32_e32 v47, v47
	s_nop 0
	v_mul_f32_e32 v47, v47, v49
	v_mul_f32_e32 v33, v47, v33
	v_fmac_f32_e32 v90, v33, v33
	s_waitcnt vmcnt(4)
	v_lshlrev_b32_e32 v66, 16, v217
	v_and_b32_e32 v67, 0xffff0000, v217
	v_add3_u32 v49, v93, v68, v91
	ds_read_u16 v49, v49 offset:8192
	v_lshlrev_b32_e32 v47, 16, v216
	v_and_b32_e32 v48, 0xffff0000, v216
	s_waitcnt lgkmcnt(0)
	v_lshlrev_b32_e32 v49, 16, v49
	v_fma_f32 v2, v46, v49, v2
	v_mul_f32_e32 v49, 0xbfb8aa3b, v47
	v_exp_f32_e32 v49, v49
	s_nop 0
	v_add_f32_e32 v49, 1.0, v49
	v_rcp_f32_e32 v49, v49
	s_nop 0
	v_mul_f32_e32 v47, v49, v47
	v_mul_f32_e32 v47, v2, v47
	v_add3_u32 v2, v94, v68, v91
	ds_read_u16 v2, v2 offset:8448
	v_fmac_f32_e32 v90, v47, v47
	s_waitcnt lgkmcnt(0)
	v_lshlrev_b32_e32 v2, 16, v2
	v_fma_f32 v2, v46, v2, v3
	v_mul_f32_e32 v3, 0xbfb8aa3b, v48
	v_exp_f32_e32 v3, v3
	s_nop 0
	v_add_f32_e32 v3, 1.0, v3
	v_rcp_f32_e32 v3, v3
	s_nop 0
	v_mul_f32_e32 v3, v3, v48
	v_mul_f32_e32 v48, v2, v3
	v_mul_f32_e32 v3, 0xbfb8aa3b, v66
	v_exp_f32_e32 v3, v3
	v_add3_u32 v2, v95, v68, v91
	ds_read_u16 v2, v2 offset:8704
	v_fmac_f32_e32 v90, v48, v48
	v_add_f32_e32 v3, 1.0, v3
	v_rcp_f32_e32 v3, v3
	s_waitcnt lgkmcnt(0)
	v_lshlrev_b32_e32 v2, 16, v2
	v_fma_f32 v2, v46, v2, v4
	v_mul_f32_e32 v3, v3, v66
	v_mul_f32_e32 v49, v2, v3
	v_mul_f32_e32 v3, 0xbfb8aa3b, v67
	v_exp_f32_e32 v3, v3
	v_add3_u32 v2, v96, v68, v91
	ds_read_u16 v2, v2 offset:8960
	v_fmac_f32_e32 v90, v49, v49
	v_add_f32_e32 v3, 1.0, v3
	v_rcp_f32_e32 v3, v3
	s_nop 0
	v_mul_f32_e32 v3, v3, v67
	v_add_lshl_u32 v67, v64, s12, 8
	v_add3_u32 v64, v65, v67, v91
	ds_read_u16 v64, v64 offset:8192
	s_waitcnt lgkmcnt(1)
	v_lshlrev_b32_e32 v2, 16, v2
	v_fma_f32 v2, v46, v2, v5
	v_mul_f32_e32 v66, v3, v2
	s_waitcnt lgkmcnt(0)
	v_lshlrev_b32_e32 v64, 16, v64
	v_fma_f32 v6, v46, v64, v6
	v_fmac_f32_e32 v90, v66, v66
	s_waitcnt vmcnt(3)
	v_lshlrev_b32_e32 v4, 16, v218
	v_mul_f32_e32 v64, 0xbfb8aa3b, v4
	v_exp_f32_e32 v64, v64
	v_and_b32_e32 v2, 0xffff0000, v218
	v_lshlrev_b32_e32 v5, 16, v219
	v_and_b32_e32 v3, 0xffff0000, v219
	v_add_f32_e32 v64, 1.0, v64
	v_rcp_f32_e32 v64, v64
	s_nop 0
	v_mul_f32_e32 v4, v64, v4
	v_mul_f32_e32 v64, v6, v4
	v_mul_f32_e32 v6, 0xbfb8aa3b, v2
	v_exp_f32_e32 v6, v6
	v_add3_u32 v4, v97, v67, v91
	ds_read_u16 v4, v4 offset:8448
	v_fmac_f32_e32 v90, v64, v64
	v_add_f32_e32 v6, 1.0, v6
	v_rcp_f32_e32 v6, v6
	s_waitcnt lgkmcnt(0)
	v_lshlrev_b32_e32 v4, 16, v4
	v_fma_f32 v4, v46, v4, v7
	v_mul_f32_e32 v2, v6, v2
	v_mul_f32_e32 v65, v4, v2
	v_mul_f32_e32 v4, 0xbfb8aa3b, v5
	v_exp_f32_e32 v4, v4
	v_add3_u32 v2, v98, v67, v91
	ds_read_u16 v2, v2 offset:8704
	v_add_lshl_u32 v6, v63, s12, 8
	v_add_f32_e32 v4, 1.0, v4
	v_rcp_f32_e32 v4, v4
	v_add3_u32 v7, v93, v6, v91
	ds_read_u16 v7, v7 offset:8192
	s_waitcnt lgkmcnt(1)
	v_lshlrev_b32_e32 v2, 16, v2
	v_fma_f32 v2, v46, v2, v8
	v_mul_f32_e32 v4, v4, v5
	v_mul_f32_e32 v8, v2, v4
	v_mul_f32_e32 v4, 0xbfb8aa3b, v3
	v_exp_f32_e32 v4, v4
	v_add3_u32 v2, v99, v67, v91
	ds_read_u16 v2, v2 offset:8960
	s_waitcnt lgkmcnt(1)
	v_lshlrev_b32_e32 v7, 16, v7
	v_add_f32_e32 v4, 1.0, v4
	v_rcp_f32_e32 v4, v4
	v_fma_f32 v7, v46, v7, v10
	s_waitcnt lgkmcnt(0)
	v_lshlrev_b32_e32 v2, 16, v2
	v_fma_f32 v2, v46, v2, v9
	v_mul_f32_e32 v3, v4, v3
	v_mul_f32_e32 v9, v3, v2
	v_fmac_f32_e32 v90, v65, v65
	v_fmac_f32_e32 v90, v8, v8
	v_fmac_f32_e32 v90, v9, v9
	s_waitcnt vmcnt(2)
	v_lshlrev_b32_e32 v4, 16, v220
	v_mul_f32_e32 v10, 0xbfb8aa3b, v4
	v_exp_f32_e32 v10, v10
	v_and_b32_e32 v2, 0xffff0000, v220
	v_lshlrev_b32_e32 v5, 16, v221
	v_and_b32_e32 v3, 0xffff0000, v221
	v_add_f32_e32 v10, 1.0, v10
	v_rcp_f32_e32 v10, v10
	s_nop 0
	v_mul_f32_e32 v4, v10, v4
	v_mul_f32_e32 v10, v7, v4
	v_mul_f32_e32 v7, 0xbfb8aa3b, v2
	v_exp_f32_e32 v7, v7
	v_add3_u32 v4, v94, v6, v91
	ds_read_u16 v4, v4 offset:8448
	v_fmac_f32_e32 v90, v10, v10
	v_add_f32_e32 v7, 1.0, v7
	v_rcp_f32_e32 v7, v7
	s_waitcnt lgkmcnt(0)
	v_lshlrev_b32_e32 v4, 16, v4
	v_fma_f32 v4, v46, v4, v11
	v_mul_f32_e32 v2, v7, v2
	v_mul_f32_e32 v11, v4, v2
	v_mul_f32_e32 v4, 0xbfb8aa3b, v5
	v_exp_f32_e32 v4, v4
	v_add3_u32 v2, v95, v6, v91
	ds_read_u16 v2, v2 offset:8704
	v_fmac_f32_e32 v90, v11, v11
	v_add_f32_e32 v4, 1.0, v4
	v_rcp_f32_e32 v4, v4
	s_waitcnt lgkmcnt(0)
	v_lshlrev_b32_e32 v2, 16, v2
	v_fma_f32 v2, v46, v2, v12
	v_mul_f32_e32 v4, v4, v5
	v_mul_f32_e32 v12, v2, v4
	v_mul_f32_e32 v4, 0xbfb8aa3b, v3
	v_exp_f32_e32 v4, v4
	v_add3_u32 v2, v96, v6, v91
	ds_read_u16 v2, v2 offset:8960
	v_fmac_f32_e32 v90, v12, v12
	v_add_f32_e32 v4, 1.0, v4
	v_rcp_f32_e32 v4, v4
	s_waitcnt lgkmcnt(0)
	v_lshlrev_b32_e32 v2, 16, v2
	v_fma_f32 v2, v46, v2, v13
	v_mul_f32_e32 v3, v4, v3
	v_mul_f32_e32 v13, v3, v2
	v_fmac_f32_e32 v90, v13, v13
	s_waitcnt vmcnt(1)
	v_lshlrev_b32_e32 v3, 16, v223
	v_and_b32_e32 v2, 0xffff0000, v223
	v_add_lshl_u32 v5, v92, s12, 8
	v_add3_u32 v7, v62, v5, v91
	ds_read_u16 v7, v7 offset:8192
	v_lshlrev_b32_e32 v6, 16, v222
	v_and_b32_e32 v4, 0xffff0000, v222
	s_waitcnt lgkmcnt(0)
	v_lshlrev_b32_e32 v7, 16, v7
	v_fma_f32 v7, v46, v7, v14
	v_mul_f32_e32 v14, 0xbfb8aa3b, v6
	v_exp_f32_e32 v14, v14
	s_nop 0
	v_add_f32_e32 v14, 1.0, v14
	v_rcp_f32_e32 v14, v14
	s_nop 0
	v_mul_f32_e32 v6, v14, v6
	v_mul_f32_e32 v14, v7, v6
	v_mul_f32_e32 v7, 0xbfb8aa3b, v4
	v_exp_f32_e32 v7, v7
	v_add3_u32 v6, v45, v5, v91
	ds_read_u16 v6, v6 offset:8448
	v_fmac_f32_e32 v90, v14, v14
	v_add_f32_e32 v7, 1.0, v7
	v_rcp_f32_e32 v7, v7
	s_waitcnt lgkmcnt(0)
	v_lshlrev_b32_e32 v6, 16, v6
	v_fma_f32 v6, v46, v6, v15
	v_mul_f32_e32 v4, v7, v4
	v_mul_f32_e32 v15, v6, v4
	v_mul_f32_e32 v6, 0xbfb8aa3b, v3
	v_exp_f32_e32 v6, v6
	v_add3_u32 v4, v44, v5, v91
	ds_read_u16 v4, v4 offset:8704
	v_fmac_f32_e32 v90, v15, v15
	v_add_f32_e32 v6, 1.0, v6
	v_rcp_f32_e32 v6, v6
	s_waitcnt lgkmcnt(0)
	v_lshlrev_b32_e32 v4, 16, v4
	v_fma_f32 v4, v46, v4, v16
	v_mul_f32_e32 v3, v6, v3
	v_mul_f32_e32 v16, v4, v3
	v_add3_u32 v3, v43, v5, v91
	ds_read_u16 v3, v3 offset:8960
	v_fmac_f32_e32 v90, v16, v16
	s_waitcnt lgkmcnt(0)
	v_lshlrev_b32_e32 v3, 16, v3
	v_fmac_f32_e32 v17, v46, v3
	v_mul_f32_e32 v3, 0xbfb8aa3b, v2
	v_exp_f32_e32 v3, v3
	s_nop 0
	v_add_f32_e32 v3, 1.0, v3
	v_rcp_f32_e32 v3, v3
	s_nop 0
	v_mul_f32_e32 v2, v3, v2
	v_mul_f32_e32 v17, v2, v17
	v_fmac_f32_e32 v90, v17, v17
	v_mov_b32_e32 v2, v90
	s_nop 1
	v_permlane32_swap_b32_e32 v90, v2
	s_and_saveexec_b64 s[38:39], vcc
	s_cbranch_execz .LBB0_529
	v_readlane_b32 s12, v253, 40
	v_add_f32_e32 v2, v90, v2
	s_nop 0
	v_lshl_add_u32 v3, v87, 2, s12
	ds_write_b32 v3, v2 offset:4352
	s_branch .LBB0_529
